# attention epilogue: store tail widened, 64 global_store_byte per lane -> 16 global_store_dword via quad DPP + v_perm_b32 4x4 byte transpose (full 128-B row segments per store)
# speedup vs baseline: 1.0081x; 1.0081x over previous
.LBB0_746:
	s_or_b64 exec, exec, s[6:7]
	s_waitcnt lgkmcnt(0)
	v_add_u32_e32 v72, s62, v169
	ds_read_b128 v[224:227], v72
	ds_read_b128 v[228:231], v72 offset:32
	ds_read_b128 v[232:235], v72 offset:64
	ds_read_b128 v[236:239], v72 offset:96
	s_lshl_b64 s[6:7], s[30:31], 11
	s_add_u32 s6, s43, s6
	s_addc_u32 s7, s44, s7
	s_add_u32 s8, s6, s61
	s_addc_u32 s9, s7, 0
	v_and_b32_e32 v240, 3, v254
	v_bfe_u32 v241, v254, 2, 3
	v_readfirstlane_b32 s6, v254
	s_ashr_i32 s6, s6, 1
	s_andn2_b32 s6, s6, 31
	s_ashr_i32 s7, s6, 31
	s_lshl_b64 s[6:7], s[6:7], 11
	s_add_u32 s6, s8, s6
	s_addc_u32 s7, s9, s7
	v_lshlrev_b32_e32 v240, 5, v240
	v_lshl_or_b32 v140, v241, 2, v240
	v_lshlrev_b32_e32 v241, 8, v254
	v_and_b32_e32 v241, 0x2000, v241
	v_or_b32_e32 v140, v140, v241
	v_or_b32_e32 v140, 0x1000, v140
	v_mov_b32_e32 v242, 0x4000
	v_mov_b32_e32 v243, 0
	v_and_b32_e32 v244, 1, v254
	v_bfe_u32 v245, v254, 1, 1
	v_sub_u32_e32 v244, 0, v244
	v_sub_u32_e32 v245, 0, v245
	v_and_b32_e32 v244, 0x05050505, v244
	v_and_b32_e32 v245, 0x06060606, v245
	v_xor_b32_e32 v244, 0x06020400, v244
	v_xor_b32_e32 v245, 0x05040100, v245
	v_lshl_add_u64 v[64:65], s[6:7], 0, v[140:141]
	v_lshl_add_u64 v[66:67], v[64:65], 0, v[242:243]
	v_lshl_add_u64 v[68:69], v[66:67], 0, v[242:243]
	v_lshl_add_u64 v[70:71], v[68:69], 0, v[242:243]
	s_waitcnt lgkmcnt(0)
	v_rcp_f32_e32 v224, v224
	v_rcp_f32_e32 v225, v225
	v_rcp_f32_e32 v226, v226
	v_rcp_f32_e32 v227, v227
	v_rcp_f32_e32 v228, v228
	v_rcp_f32_e32 v229, v229
	v_rcp_f32_e32 v230, v230
	v_rcp_f32_e32 v231, v231
	v_rcp_f32_e32 v232, v232
	v_rcp_f32_e32 v233, v233
	v_rcp_f32_e32 v234, v234
	v_rcp_f32_e32 v235, v235
	v_rcp_f32_e32 v236, v236
	v_rcp_f32_e32 v237, v237
	v_rcp_f32_e32 v238, v238
	v_rcp_f32_e32 v239, v239
	v_mul_f32_e32 v16, v16, v224
	v_mul_f32_e32 v32, v32, v224
	v_mul_f32_e32 v0, v0, v224
	v_mul_f32_e32 v48, v48, v224
	v_mul_f32_e32 v17, v17, v225
	v_mul_f32_e32 v33, v33, v225
	v_mul_f32_e32 v1, v1, v225
	v_mul_f32_e32 v49, v49, v225
	v_mul_f32_e32 v18, v18, v226
	v_mul_f32_e32 v34, v34, v226
	v_mul_f32_e32 v2, v2, v226
	v_mul_f32_e32 v50, v50, v226
	v_mul_f32_e32 v19, v19, v227
	v_mul_f32_e32 v35, v35, v227
	v_mul_f32_e32 v3, v3, v227
	v_mul_f32_e32 v51, v51, v227
	v_cvt_pk_fp8_f32 v246, v16, v32
	v_cvt_pk_fp8_f32 v246, v0, v48 op_sel:[0,0,1]
	v_cvt_pk_fp8_f32 v247, v17, v33
	v_cvt_pk_fp8_f32 v247, v1, v49 op_sel:[0,0,1]
	v_cvt_pk_fp8_f32 v248, v18, v34
	v_cvt_pk_fp8_f32 v248, v2, v50 op_sel:[0,0,1]
	v_cvt_pk_fp8_f32 v249, v19, v35
	v_cvt_pk_fp8_f32 v249, v3, v51 op_sel:[0,0,1]
	s_nop 1
	v_mov_b32_dpp v250, v246 quad_perm:[1,0,3,2] row_mask:0xf bank_mask:0xf
	v_mov_b32_dpp v251, v247 quad_perm:[1,0,3,2] row_mask:0xf bank_mask:0xf
	v_mov_b32_dpp v252, v248 quad_perm:[1,0,3,2] row_mask:0xf bank_mask:0xf
	v_mov_b32_dpp v253, v249 quad_perm:[1,0,3,2] row_mask:0xf bank_mask:0xf
	s_nop 0
	v_perm_b32 v246, v250, v246, v244
	v_perm_b32 v247, v251, v247, v244
	v_perm_b32 v248, v252, v248, v244
	v_perm_b32 v249, v253, v249, v244
	s_nop 1
	v_mov_b32_dpp v250, v246 quad_perm:[2,3,0,1] row_mask:0xf bank_mask:0xf
	v_mov_b32_dpp v251, v247 quad_perm:[2,3,0,1] row_mask:0xf bank_mask:0xf
	v_mov_b32_dpp v252, v248 quad_perm:[2,3,0,1] row_mask:0xf bank_mask:0xf
	v_mov_b32_dpp v253, v249 quad_perm:[2,3,0,1] row_mask:0xf bank_mask:0xf
	s_nop 0
	v_perm_b32 v246, v250, v246, v245
	v_perm_b32 v247, v251, v247, v245
	v_perm_b32 v248, v252, v248, v245
	v_perm_b32 v249, v253, v249, v245
	global_store_dword v[64:65], v246, off offset:-4096
	global_store_dword v[64:65], v247, off offset:-2048
	global_store_dword v[64:65], v248, off
	global_store_dword v[64:65], v249, off offset:2048
	s_nop 1
	v_mul_f32_e32 v20, v20, v228
	v_mul_f32_e32 v36, v36, v228
	v_mul_f32_e32 v4, v4, v228
	v_mul_f32_e32 v52, v52, v228
	v_mul_f32_e32 v21, v21, v229
	v_mul_f32_e32 v37, v37, v229
	v_mul_f32_e32 v5, v5, v229
	v_mul_f32_e32 v53, v53, v229
	v_mul_f32_e32 v22, v22, v230
	v_mul_f32_e32 v38, v38, v230
	v_mul_f32_e32 v6, v6, v230
	v_mul_f32_e32 v54, v54, v230
	v_mul_f32_e32 v23, v23, v231
	v_mul_f32_e32 v39, v39, v231
	v_mul_f32_e32 v7, v7, v231
	v_mul_f32_e32 v55, v55, v231
	v_cvt_pk_fp8_f32 v246, v20, v36
	v_cvt_pk_fp8_f32 v246, v4, v52 op_sel:[0,0,1]
	v_cvt_pk_fp8_f32 v247, v21, v37
	v_cvt_pk_fp8_f32 v247, v5, v53 op_sel:[0,0,1]
	v_cvt_pk_fp8_f32 v248, v22, v38
	v_cvt_pk_fp8_f32 v248, v6, v54 op_sel:[0,0,1]
	v_cvt_pk_fp8_f32 v249, v23, v39
	v_cvt_pk_fp8_f32 v249, v7, v55 op_sel:[0,0,1]
	s_nop 1
	v_mov_b32_dpp v250, v246 quad_perm:[1,0,3,2] row_mask:0xf bank_mask:0xf
	v_mov_b32_dpp v251, v247 quad_perm:[1,0,3,2] row_mask:0xf bank_mask:0xf
	v_mov_b32_dpp v252, v248 quad_perm:[1,0,3,2] row_mask:0xf bank_mask:0xf
	v_mov_b32_dpp v253, v249 quad_perm:[1,0,3,2] row_mask:0xf bank_mask:0xf
	s_nop 0
	v_perm_b32 v246, v250, v246, v244
	v_perm_b32 v247, v251, v247, v244
	v_perm_b32 v248, v252, v248, v244
	v_perm_b32 v249, v253, v249, v244
	s_nop 1
	v_mov_b32_dpp v250, v246 quad_perm:[2,3,0,1] row_mask:0xf bank_mask:0xf
	v_mov_b32_dpp v251, v247 quad_perm:[2,3,0,1] row_mask:0xf bank_mask:0xf
	v_mov_b32_dpp v252, v248 quad_perm:[2,3,0,1] row_mask:0xf bank_mask:0xf
	v_mov_b32_dpp v253, v249 quad_perm:[2,3,0,1] row_mask:0xf bank_mask:0xf
	s_nop 0
	v_perm_b32 v246, v250, v246, v245
	v_perm_b32 v247, v251, v247, v245
	v_perm_b32 v248, v252, v248, v245
	v_perm_b32 v249, v253, v249, v245
	global_store_dword v[66:67], v246, off offset:-4096
	global_store_dword v[66:67], v247, off offset:-2048
	global_store_dword v[66:67], v248, off
	global_store_dword v[66:67], v249, off offset:2048
	s_nop 1
	v_mul_f32_e32 v24, v24, v232
	v_mul_f32_e32 v40, v40, v232
	v_mul_f32_e32 v8, v8, v232
	v_mul_f32_e32 v56, v56, v232
	v_mul_f32_e32 v25, v25, v233
	v_mul_f32_e32 v41, v41, v233
	v_mul_f32_e32 v9, v9, v233
	v_mul_f32_e32 v57, v57, v233
	v_mul_f32_e32 v26, v26, v234
	v_mul_f32_e32 v42, v42, v234
	v_mul_f32_e32 v10, v10, v234
	v_mul_f32_e32 v58, v58, v234
	v_mul_f32_e32 v27, v27, v235
	v_mul_f32_e32 v43, v43, v235
	v_mul_f32_e32 v11, v11, v235
	v_mul_f32_e32 v59, v59, v235
	v_cvt_pk_fp8_f32 v246, v24, v40
	v_cvt_pk_fp8_f32 v246, v8, v56 op_sel:[0,0,1]
	v_cvt_pk_fp8_f32 v247, v25, v41
	v_cvt_pk_fp8_f32 v247, v9, v57 op_sel:[0,0,1]
	v_cvt_pk_fp8_f32 v248, v26, v42
	v_cvt_pk_fp8_f32 v248, v10, v58 op_sel:[0,0,1]
	v_cvt_pk_fp8_f32 v249, v27, v43
	v_cvt_pk_fp8_f32 v249, v11, v59 op_sel:[0,0,1]
	s_nop 1
	v_mov_b32_dpp v250, v246 quad_perm:[1,0,3,2] row_mask:0xf bank_mask:0xf
	v_mov_b32_dpp v251, v247 quad_perm:[1,0,3,2] row_mask:0xf bank_mask:0xf
	v_mov_b32_dpp v252, v248 quad_perm:[1,0,3,2] row_mask:0xf bank_mask:0xf
	v_mov_b32_dpp v253, v249 quad_perm:[1,0,3,2] row_mask:0xf bank_mask:0xf
	s_nop 0
	v_perm_b32 v246, v250, v246, v244
	v_perm_b32 v247, v251, v247, v244
	v_perm_b32 v248, v252, v248, v244
	v_perm_b32 v249, v253, v249, v244
	s_nop 1
	v_mov_b32_dpp v250, v246 quad_perm:[2,3,0,1] row_mask:0xf bank_mask:0xf
	v_mov_b32_dpp v251, v247 quad_perm:[2,3,0,1] row_mask:0xf bank_mask:0xf
	v_mov_b32_dpp v252, v248 quad_perm:[2,3,0,1] row_mask:0xf bank_mask:0xf
	v_mov_b32_dpp v253, v249 quad_perm:[2,3,0,1] row_mask:0xf bank_mask:0xf
	s_nop 0
	v_perm_b32 v246, v250, v246, v245
	v_perm_b32 v247, v251, v247, v245
	v_perm_b32 v248, v252, v248, v245
	v_perm_b32 v249, v253, v249, v245
	global_store_dword v[68:69], v246, off offset:-4096
	global_store_dword v[68:69], v247, off offset:-2048
	global_store_dword v[68:69], v248, off
	global_store_dword v[68:69], v249, off offset:2048
	s_nop 1
	v_mul_f32_e32 v28, v28, v236
	v_mul_f32_e32 v44, v44, v236
	v_mul_f32_e32 v12, v12, v236
	v_mul_f32_e32 v60, v60, v236
	v_mul_f32_e32 v29, v29, v237
	v_mul_f32_e32 v45, v45, v237
	v_mul_f32_e32 v13, v13, v237
	v_mul_f32_e32 v61, v61, v237
	v_mul_f32_e32 v30, v30, v238
	v_mul_f32_e32 v46, v46, v238
	v_mul_f32_e32 v14, v14, v238
	v_mul_f32_e32 v62, v62, v238
	v_mul_f32_e32 v31, v31, v239
	v_mul_f32_e32 v47, v47, v239
	v_mul_f32_e32 v15, v15, v239
	v_mul_f32_e32 v63, v63, v239
	v_cvt_pk_fp8_f32 v246, v28, v44
	v_cvt_pk_fp8_f32 v246, v12, v60 op_sel:[0,0,1]
	v_cvt_pk_fp8_f32 v247, v29, v45
	v_cvt_pk_fp8_f32 v247, v13, v61 op_sel:[0,0,1]
	v_cvt_pk_fp8_f32 v248, v30, v46
	v_cvt_pk_fp8_f32 v248, v14, v62 op_sel:[0,0,1]
	v_cvt_pk_fp8_f32 v249, v31, v47
	v_cvt_pk_fp8_f32 v249, v15, v63 op_sel:[0,0,1]
	s_nop 1
	v_mov_b32_dpp v250, v246 quad_perm:[1,0,3,2] row_mask:0xf bank_mask:0xf
	v_mov_b32_dpp v251, v247 quad_perm:[1,0,3,2] row_mask:0xf bank_mask:0xf
	v_mov_b32_dpp v252, v248 quad_perm:[1,0,3,2] row_mask:0xf bank_mask:0xf
	v_mov_b32_dpp v253, v249 quad_perm:[1,0,3,2] row_mask:0xf bank_mask:0xf
	s_nop 0
	v_perm_b32 v246, v250, v246, v244
	v_perm_b32 v247, v251, v247, v244
	v_perm_b32 v248, v252, v248, v244
	v_perm_b32 v249, v253, v249, v244
	s_nop 1
	v_mov_b32_dpp v250, v246 quad_perm:[2,3,0,1] row_mask:0xf bank_mask:0xf
	v_mov_b32_dpp v251, v247 quad_perm:[2,3,0,1] row_mask:0xf bank_mask:0xf
	v_mov_b32_dpp v252, v248 quad_perm:[2,3,0,1] row_mask:0xf bank_mask:0xf
	v_mov_b32_dpp v253, v249 quad_perm:[2,3,0,1] row_mask:0xf bank_mask:0xf
	s_nop 0
	v_perm_b32 v246, v250, v246, v245
	v_perm_b32 v247, v251, v247, v245
	v_perm_b32 v248, v252, v248, v245
	v_perm_b32 v249, v253, v249, v245
	global_store_dword v[70:71], v246, off offset:-4096
	global_store_dword v[70:71], v247, off offset:-2048
	global_store_dword v[70:71], v248, off
	global_store_dword v[70:71], v249, off offset:2048
	s_nop 1
	s_add_i32 s36, s36, s29
	s_cmpk_lt_i32 s36, 0x220
	s_waitcnt vmcnt(63) expcnt(7) lgkmcnt(15)
	s_barrier
	s_cbranch_scc0 .LBB0_773

.LBB0_2006:
	s_or_b64 exec, exec, s[6:7]
	s_waitcnt lgkmcnt(0)
	v_add_u32_e32 v72, s12, v169
	ds_read_b128 v[224:227], v72
	ds_read_b128 v[228:231], v72 offset:32
	ds_read_b128 v[232:235], v72 offset:64
	ds_read_b128 v[236:239], v72 offset:96
	s_lshl_b64 s[6:7], s[28:29], 11
	s_add_u32 s6, s41, s6
	s_addc_u32 s7, s42, s7
	s_add_u32 s8, s6, s59
	s_addc_u32 s10, s7, 0
	v_and_b32_e32 v240, 3, v254
	v_bfe_u32 v241, v254, 2, 3
	v_readfirstlane_b32 s6, v254
	s_ashr_i32 s6, s6, 1
	s_andn2_b32 s6, s6, 31
	s_ashr_i32 s7, s6, 31
	s_lshl_b64 s[6:7], s[6:7], 11
	s_add_u32 s6, s8, s6
	s_addc_u32 s7, s10, s7
	v_lshlrev_b32_e32 v240, 5, v240
	v_lshl_or_b32 v140, v241, 2, v240
	v_lshlrev_b32_e32 v241, 8, v254
	v_and_b32_e32 v241, 0x2000, v241
	v_or_b32_e32 v140, v140, v241
	v_or_b32_e32 v140, 0x1000, v140
	v_mov_b32_e32 v242, 0x4000
	v_mov_b32_e32 v243, 0
	v_and_b32_e32 v244, 1, v254
	v_bfe_u32 v245, v254, 1, 1
	v_sub_u32_e32 v244, 0, v244
	v_sub_u32_e32 v245, 0, v245
	v_and_b32_e32 v244, 0x05050505, v244
	v_and_b32_e32 v245, 0x06060606, v245
	v_xor_b32_e32 v244, 0x06020400, v244
	v_xor_b32_e32 v245, 0x05040100, v245
	v_lshl_add_u64 v[64:65], s[6:7], 0, v[140:141]
	v_lshl_add_u64 v[66:67], v[64:65], 0, v[242:243]
	v_lshl_add_u64 v[68:69], v[66:67], 0, v[242:243]
	v_lshl_add_u64 v[70:71], v[68:69], 0, v[242:243]
	s_waitcnt lgkmcnt(0)
	v_rcp_f32_e32 v224, v224
	v_rcp_f32_e32 v225, v225
	v_rcp_f32_e32 v226, v226
	v_rcp_f32_e32 v227, v227
	v_rcp_f32_e32 v228, v228
	v_rcp_f32_e32 v229, v229
	v_rcp_f32_e32 v230, v230
	v_rcp_f32_e32 v231, v231
	v_rcp_f32_e32 v232, v232
	v_rcp_f32_e32 v233, v233
	v_rcp_f32_e32 v234, v234
	v_rcp_f32_e32 v235, v235
	v_rcp_f32_e32 v236, v236
	v_rcp_f32_e32 v237, v237
	v_rcp_f32_e32 v238, v238
	v_rcp_f32_e32 v239, v239
	v_mul_f32_e32 v0, v0, v224
	v_mul_f32_e32 v32, v32, v224
	v_mul_f32_e32 v16, v16, v224
	v_mul_f32_e32 v48, v48, v224
	v_mul_f32_e32 v1, v1, v225
	v_mul_f32_e32 v33, v33, v225
	v_mul_f32_e32 v17, v17, v225
	v_mul_f32_e32 v49, v49, v225
	v_mul_f32_e32 v2, v2, v226
	v_mul_f32_e32 v34, v34, v226
	v_mul_f32_e32 v18, v18, v226
	v_mul_f32_e32 v50, v50, v226
	v_mul_f32_e32 v3, v3, v227
	v_mul_f32_e32 v35, v35, v227
	v_mul_f32_e32 v19, v19, v227
	v_mul_f32_e32 v51, v51, v227
	v_cvt_pk_fp8_f32 v246, v0, v32
	v_cvt_pk_fp8_f32 v246, v16, v48 op_sel:[0,0,1]
	v_cvt_pk_fp8_f32 v247, v1, v33
	v_cvt_pk_fp8_f32 v247, v17, v49 op_sel:[0,0,1]
	v_cvt_pk_fp8_f32 v248, v2, v34
	v_cvt_pk_fp8_f32 v248, v18, v50 op_sel:[0,0,1]
	v_cvt_pk_fp8_f32 v249, v3, v35
	v_cvt_pk_fp8_f32 v249, v19, v51 op_sel:[0,0,1]
	s_nop 1
	v_mov_b32_dpp v250, v246 quad_perm:[1,0,3,2] row_mask:0xf bank_mask:0xf
	v_mov_b32_dpp v251, v247 quad_perm:[1,0,3,2] row_mask:0xf bank_mask:0xf
	v_mov_b32_dpp v252, v248 quad_perm:[1,0,3,2] row_mask:0xf bank_mask:0xf
	v_mov_b32_dpp v253, v249 quad_perm:[1,0,3,2] row_mask:0xf bank_mask:0xf
	s_nop 0
	v_perm_b32 v246, v250, v246, v244
	v_perm_b32 v247, v251, v247, v244
	v_perm_b32 v248, v252, v248, v244
	v_perm_b32 v249, v253, v249, v244
	s_nop 1
	v_mov_b32_dpp v250, v246 quad_perm:[2,3,0,1] row_mask:0xf bank_mask:0xf
	v_mov_b32_dpp v251, v247 quad_perm:[2,3,0,1] row_mask:0xf bank_mask:0xf
	v_mov_b32_dpp v252, v248 quad_perm:[2,3,0,1] row_mask:0xf bank_mask:0xf
	v_mov_b32_dpp v253, v249 quad_perm:[2,3,0,1] row_mask:0xf bank_mask:0xf
	s_nop 0
	v_perm_b32 v246, v250, v246, v245
	v_perm_b32 v247, v251, v247, v245
	v_perm_b32 v248, v252, v248, v245
	v_perm_b32 v249, v253, v249, v245
	global_store_dword v[64:65], v246, off offset:-4096
	global_store_dword v[64:65], v247, off offset:-2048
	global_store_dword v[64:65], v248, off
	global_store_dword v[64:65], v249, off offset:2048
	s_nop 1
	v_mul_f32_e32 v4, v4, v228
	v_mul_f32_e32 v36, v36, v228
	v_mul_f32_e32 v20, v20, v228
	v_mul_f32_e32 v52, v52, v228
	v_mul_f32_e32 v5, v5, v229
	v_mul_f32_e32 v37, v37, v229
	v_mul_f32_e32 v21, v21, v229
	v_mul_f32_e32 v53, v53, v229
	v_mul_f32_e32 v6, v6, v230
	v_mul_f32_e32 v38, v38, v230
	v_mul_f32_e32 v22, v22, v230
	v_mul_f32_e32 v54, v54, v230
	v_mul_f32_e32 v7, v7, v231
	v_mul_f32_e32 v39, v39, v231
	v_mul_f32_e32 v23, v23, v231
	v_mul_f32_e32 v55, v55, v231
	v_cvt_pk_fp8_f32 v246, v4, v36
	v_cvt_pk_fp8_f32 v246, v20, v52 op_sel:[0,0,1]
	v_cvt_pk_fp8_f32 v247, v5, v37
	v_cvt_pk_fp8_f32 v247, v21, v53 op_sel:[0,0,1]
	v_cvt_pk_fp8_f32 v248, v6, v38
	v_cvt_pk_fp8_f32 v248, v22, v54 op_sel:[0,0,1]
	v_cvt_pk_fp8_f32 v249, v7, v39
	v_cvt_pk_fp8_f32 v249, v23, v55 op_sel:[0,0,1]
	s_nop 1
	v_mov_b32_dpp v250, v246 quad_perm:[1,0,3,2] row_mask:0xf bank_mask:0xf
	v_mov_b32_dpp v251, v247 quad_perm:[1,0,3,2] row_mask:0xf bank_mask:0xf
	v_mov_b32_dpp v252, v248 quad_perm:[1,0,3,2] row_mask:0xf bank_mask:0xf
	v_mov_b32_dpp v253, v249 quad_perm:[1,0,3,2] row_mask:0xf bank_mask:0xf
	s_nop 0
	v_perm_b32 v246, v250, v246, v244
	v_perm_b32 v247, v251, v247, v244
	v_perm_b32 v248, v252, v248, v244
	v_perm_b32 v249, v253, v249, v244
	s_nop 1
	v_mov_b32_dpp v250, v246 quad_perm:[2,3,0,1] row_mask:0xf bank_mask:0xf
	v_mov_b32_dpp v251, v247 quad_perm:[2,3,0,1] row_mask:0xf bank_mask:0xf
	v_mov_b32_dpp v252, v248 quad_perm:[2,3,0,1] row_mask:0xf bank_mask:0xf
	v_mov_b32_dpp v253, v249 quad_perm:[2,3,0,1] row_mask:0xf bank_mask:0xf
	s_nop 0
	v_perm_b32 v246, v250, v246, v245
	v_perm_b32 v247, v251, v247, v245
	v_perm_b32 v248, v252, v248, v245
	v_perm_b32 v249, v253, v249, v245
	global_store_dword v[66:67], v246, off offset:-4096
	global_store_dword v[66:67], v247, off offset:-2048
	global_store_dword v[66:67], v248, off
	global_store_dword v[66:67], v249, off offset:2048
	s_nop 1
	v_mul_f32_e32 v8, v8, v232
	v_mul_f32_e32 v40, v40, v232
	v_mul_f32_e32 v24, v24, v232
	v_mul_f32_e32 v56, v56, v232
	v_mul_f32_e32 v9, v9, v233
	v_mul_f32_e32 v41, v41, v233
	v_mul_f32_e32 v25, v25, v233
	v_mul_f32_e32 v57, v57, v233
	v_mul_f32_e32 v10, v10, v234
	v_mul_f32_e32 v42, v42, v234
	v_mul_f32_e32 v26, v26, v234
	v_mul_f32_e32 v58, v58, v234
	v_mul_f32_e32 v11, v11, v235
	v_mul_f32_e32 v43, v43, v235
	v_mul_f32_e32 v27, v27, v235
	v_mul_f32_e32 v59, v59, v235
	v_cvt_pk_fp8_f32 v246, v8, v40
	v_cvt_pk_fp8_f32 v246, v24, v56 op_sel:[0,0,1]
	v_cvt_pk_fp8_f32 v247, v9, v41
	v_cvt_pk_fp8_f32 v247, v25, v57 op_sel:[0,0,1]
	v_cvt_pk_fp8_f32 v248, v10, v42
	v_cvt_pk_fp8_f32 v248, v26, v58 op_sel:[0,0,1]
	v_cvt_pk_fp8_f32 v249, v11, v43
	v_cvt_pk_fp8_f32 v249, v27, v59 op_sel:[0,0,1]
	s_nop 1
	v_mov_b32_dpp v250, v246 quad_perm:[1,0,3,2] row_mask:0xf bank_mask:0xf
	v_mov_b32_dpp v251, v247 quad_perm:[1,0,3,2] row_mask:0xf bank_mask:0xf
	v_mov_b32_dpp v252, v248 quad_perm:[1,0,3,2] row_mask:0xf bank_mask:0xf
	v_mov_b32_dpp v253, v249 quad_perm:[1,0,3,2] row_mask:0xf bank_mask:0xf
	s_nop 0
	v_perm_b32 v246, v250, v246, v244
	v_perm_b32 v247, v251, v247, v244
	v_perm_b32 v248, v252, v248, v244
	v_perm_b32 v249, v253, v249, v244
	s_nop 1
	v_mov_b32_dpp v250, v246 quad_perm:[2,3,0,1] row_mask:0xf bank_mask:0xf
	v_mov_b32_dpp v251, v247 quad_perm:[2,3,0,1] row_mask:0xf bank_mask:0xf
	v_mov_b32_dpp v252, v248 quad_perm:[2,3,0,1] row_mask:0xf bank_mask:0xf
	v_mov_b32_dpp v253, v249 quad_perm:[2,3,0,1] row_mask:0xf bank_mask:0xf
	s_nop 0
	v_perm_b32 v246, v250, v246, v245
	v_perm_b32 v247, v251, v247, v245
	v_perm_b32 v248, v252, v248, v245
	v_perm_b32 v249, v253, v249, v245
	global_store_dword v[68:69], v246, off offset:-4096
	global_store_dword v[68:69], v247, off offset:-2048
	global_store_dword v[68:69], v248, off
	global_store_dword v[68:69], v249, off offset:2048
	s_nop 1
	v_mul_f32_e32 v12, v12, v236
	v_mul_f32_e32 v44, v44, v236
	v_mul_f32_e32 v28, v28, v236
	v_mul_f32_e32 v60, v60, v236
	v_mul_f32_e32 v13, v13, v237
	v_mul_f32_e32 v45, v45, v237
	v_mul_f32_e32 v29, v29, v237
	v_mul_f32_e32 v61, v61, v237
	v_mul_f32_e32 v14, v14, v238
	v_mul_f32_e32 v46, v46, v238
	v_mul_f32_e32 v30, v30, v238
	v_mul_f32_e32 v62, v62, v238
	v_mul_f32_e32 v15, v15, v239
	v_mul_f32_e32 v47, v47, v239
	v_mul_f32_e32 v31, v31, v239
	v_mul_f32_e32 v63, v63, v239
	v_cvt_pk_fp8_f32 v246, v12, v44
	v_cvt_pk_fp8_f32 v246, v28, v60 op_sel:[0,0,1]
	v_cvt_pk_fp8_f32 v247, v13, v45
	v_cvt_pk_fp8_f32 v247, v29, v61 op_sel:[0,0,1]
	v_cvt_pk_fp8_f32 v248, v14, v46
	v_cvt_pk_fp8_f32 v248, v30, v62 op_sel:[0,0,1]
	v_cvt_pk_fp8_f32 v249, v15, v47
	v_cvt_pk_fp8_f32 v249, v31, v63 op_sel:[0,0,1]
	s_nop 1
	v_mov_b32_dpp v250, v246 quad_perm:[1,0,3,2] row_mask:0xf bank_mask:0xf
	v_mov_b32_dpp v251, v247 quad_perm:[1,0,3,2] row_mask:0xf bank_mask:0xf
	v_mov_b32_dpp v252, v248 quad_perm:[1,0,3,2] row_mask:0xf bank_mask:0xf
	v_mov_b32_dpp v253, v249 quad_perm:[1,0,3,2] row_mask:0xf bank_mask:0xf
	s_nop 0
	v_perm_b32 v246, v250, v246, v244
	v_perm_b32 v247, v251, v247, v244
	v_perm_b32 v248, v252, v248, v244
	v_perm_b32 v249, v253, v249, v244
	s_nop 1
	v_mov_b32_dpp v250, v246 quad_perm:[2,3,0,1] row_mask:0xf bank_mask:0xf
	v_mov_b32_dpp v251, v247 quad_perm:[2,3,0,1] row_mask:0xf bank_mask:0xf
	v_mov_b32_dpp v252, v248 quad_perm:[2,3,0,1] row_mask:0xf bank_mask:0xf
	v_mov_b32_dpp v253, v249 quad_perm:[2,3,0,1] row_mask:0xf bank_mask:0xf
	s_nop 0
	v_perm_b32 v246, v250, v246, v245
	v_perm_b32 v247, v251, v247, v245
	v_perm_b32 v248, v252, v248, v245
	v_perm_b32 v249, v253, v249, v245
	global_store_dword v[70:71], v246, off offset:-4096
	global_store_dword v[70:71], v247, off offset:-2048
	global_store_dword v[70:71], v248, off
	global_store_dword v[70:71], v249, off offset:2048
	s_nop 1
	s_add_i32 s34, s34, s27
	s_cmpk_lt_i32 s34, 0x200
	s_waitcnt vmcnt(63) expcnt(7) lgkmcnt(15)
	s_barrier
	s_cbranch_scc0 .LBB0_2028
